# v99 + lever 9 again: T-phase merge epilogue, the 32 z==3-only blocks (1/255 scaling, bf16 store) moved out of line with inverted branches so the z<3 epilogues fall through
# speedup vs baseline: 1.0066x; 1.0066x over previous
.LBB0_874:
	s_waitcnt vmcnt(0)
	v_cvt_f32_ubyte1_e32 v141, v156
	v_cvt_f32_ubyte0_e32 v140, v156
	v_cvt_f32_ubyte3_e32 v143, v156
	v_cvt_f32_ubyte2_e32 v142, v156
	v_cndmask_b32_e64 v156, 0, 1, s[2:3]
	v_cvt_f32_ubyte1_e32 v163, v157
	v_cvt_f32_ubyte0_e32 v162, v157
	v_cvt_f32_ubyte3_e32 v167, v157
	v_cvt_f32_ubyte2_e32 v166, v157
	v_cmp_ne_u32_e64 s[42:43], 1, v156
	s_andn2_b64 vcc, exec, s[2:3]
	s_mov_b64 s[2:3], -1
	s_cbranch_vccz .Ltz3_0

.LBB0_878:
	v_lshl_add_u32 v142, s95, 8, v174
	v_ashrrev_i32_e32 v143, 31, v142
	v_lshlrev_b64 v[162:163], 11, v[142:143]
	v_lshl_or_b32 v140, s87, 8, v176
	s_cmp_eq_u32 s38, 3
	v_ashrrev_i32_e32 v141, 31, v140
	v_pk_mul_f32 v[106:107], v[106:107], v[156:157]
	v_lshl_add_u64 v[156:157], s[36:37], 0, v[162:163]
	s_cselect_b64 s[2:3], -1, 0
	s_cmp_lg_u32 s38, 3
	v_pk_mul_f32 v[108:109], v[108:109], v[168:169]
	v_pk_mul_f32 v[110:111], v[110:111], v[164:165]
	v_pk_mul_f32 v[104:105], v[104:105], v[158:159]
	v_lshl_add_u64 v[156:157], v[140:141], 1, v[156:157]
	s_cbranch_scc0 .Ltz3_1
.LBB0_880:
	v_cvt_f32_ubyte1_e32 v159, v154
	v_cvt_f32_ubyte0_e32 v158, v154
	v_cvt_f32_ubyte3_e32 v163, v154
	v_cvt_f32_ubyte2_e32 v162, v154
	v_cvt_f32_ubyte1_e32 v165, v155
	v_cvt_f32_ubyte0_e32 v164, v155
	v_cvt_f32_ubyte3_e32 v167, v155
	v_cvt_f32_ubyte2_e32 v166, v155
	s_and_b64 vcc, exec, s[42:43]
	s_mov_b64 s[22:23], -1
	s_cbranch_vccz .Ltz3_2

.LBB0_884:
	v_cndmask_b32_e64 v158, 0, 1, s[2:3]
	v_pk_mul_f32 v[76:77], v[76:77], v[172:173]
	v_pk_mul_f32 v[78:79], v[78:79], v[170:171]
	v_pk_mul_f32 v[72:73], v[72:73], v[168:169]
	v_cmp_ne_u32_e64 s[44:45], 1, v158
	s_andn2_b64 vcc, exec, s[2:3]
	v_pk_mul_f32 v[74:75], v[74:75], v[154:155]
	s_cbranch_vccz .Ltz3_3
.LBB0_886:
	v_cvt_f32_ubyte1_e32 v155, v152
	v_cvt_f32_ubyte0_e32 v154, v152
	v_cvt_f32_ubyte3_e32 v157, v152
	v_cvt_f32_ubyte2_e32 v156, v152
	v_cvt_f32_ubyte1_e32 v159, v153
	v_cvt_f32_ubyte0_e32 v158, v153
	v_cvt_f32_ubyte3_e32 v165, v153
	v_cvt_f32_ubyte2_e32 v164, v153
	s_and_b64 vcc, exec, s[42:43]
	s_mov_b64 s[2:3], -1
	s_cbranch_vccz .Ltz3_4

.LBB0_890:
	v_or_b32_e32 v154, 16, v142
	v_ashrrev_i32_e32 v155, 31, v154
	v_lshlrev_b64 v[154:155], 11, v[154:155]
	v_pk_mul_f32 v[98:99], v[98:99], v[152:153]
	v_lshl_add_u64 v[152:153], s[36:37], 0, v[154:155]
	v_pk_mul_f32 v[100:101], v[100:101], v[168:169]
	v_pk_mul_f32 v[102:103], v[102:103], v[166:167]
	v_pk_mul_f32 v[96:97], v[96:97], v[162:163]
	s_and_b64 vcc, exec, s[44:45]
	v_lshl_add_u64 v[152:153], v[140:141], 1, v[152:153]
	s_cbranch_vccz .Ltz3_5
.LBB0_892:
	s_nop 1
	v_cvt_f32_ubyte1_e32 v155, v150
	v_cvt_f32_ubyte0_e32 v154, v150
	v_cvt_f32_ubyte3_e32 v157, v150
	v_cvt_f32_ubyte2_e32 v156, v150
	v_cvt_f32_ubyte1_e32 v159, v151
	v_cvt_f32_ubyte0_e32 v158, v151
	v_cvt_f32_ubyte3_e32 v163, v151
	v_cvt_f32_ubyte2_e32 v162, v151
	s_and_b64 vcc, exec, s[42:43]
	s_mov_b64 s[2:3], -1
	s_cbranch_vccz .Ltz3_6

.LBB0_896:
	v_pk_mul_f32 v[68:69], v[68:69], v[168:169]
	v_pk_mul_f32 v[70:71], v[70:71], v[166:167]
	v_pk_mul_f32 v[64:65], v[64:65], v[164:165]
	s_and_b64 vcc, exec, s[44:45]
	v_pk_mul_f32 v[66:67], v[66:67], v[150:151]
	s_cbranch_vccz .Ltz3_7

.LBB0_908:
	s_waitcnt vmcnt(0)
	v_cvt_f32_ubyte1_e32 v157, v158
	v_cvt_f32_ubyte0_e32 v156, v158
	v_cvt_f32_ubyte3_e32 v163, v158
	v_cvt_f32_ubyte2_e32 v162, v158
	v_cvt_f32_ubyte1_e32 v165, v159
	v_cvt_f32_ubyte0_e32 v164, v159
	v_cvt_f32_ubyte3_e32 v169, v159
	v_cvt_f32_ubyte2_e32 v168, v159
	s_and_b64 vcc, exec, s[42:43]
	s_mov_b64 s[2:3], -1
	s_cbranch_vccz .Ltz3_8

.LBB0_912:
	v_or_b32_e32 v156, 32, v142
	v_ashrrev_i32_e32 v157, 31, v156
	v_lshlrev_b64 v[156:157], 11, v[156:157]
	v_lshl_add_u64 v[156:157], s[36:37], 0, v[156:157]
	v_pk_mul_f32 v[92:93], v[92:93], v[172:173]
	v_pk_mul_f32 v[94:95], v[94:95], v[170:171]
	v_pk_mul_f32 v[88:89], v[88:89], v[166:167]
	v_pk_mul_f32 v[90:91], v[90:91], v[158:159]
	s_and_b64 vcc, exec, s[44:45]
	v_lshl_add_u64 v[156:157], v[140:141], 1, v[156:157]
	s_cbranch_vccz .Ltz3_9
.LBB0_914:
	v_cvt_f32_ubyte1_e32 v159, v154
	v_cvt_f32_ubyte0_e32 v158, v154
	v_cvt_f32_ubyte3_e32 v163, v154
	v_cvt_f32_ubyte2_e32 v162, v154
	v_cvt_f32_ubyte1_e32 v165, v155
	v_cvt_f32_ubyte0_e32 v164, v155
	v_cvt_f32_ubyte3_e32 v167, v155
	v_cvt_f32_ubyte2_e32 v166, v155
	s_and_b64 vcc, exec, s[42:43]
	s_mov_b64 s[2:3], -1
	s_cbranch_vccz .Ltz3_10

.LBB0_918:
	v_pk_mul_f32 v[60:61], v[60:61], v[172:173]
	v_pk_mul_f32 v[62:63], v[62:63], v[170:171]
	v_pk_mul_f32 v[56:57], v[56:57], v[168:169]
	s_and_b64 vcc, exec, s[44:45]
	v_pk_mul_f32 v[58:59], v[58:59], v[154:155]
	s_cbranch_vccz .Ltz3_11

.LBB0_924:
	v_or_b32_e32 v154, 48, v142
	v_ashrrev_i32_e32 v155, 31, v154
	v_lshlrev_b64 v[154:155], 11, v[154:155]
	v_pk_mul_f32 v[82:83], v[82:83], v[152:153]
	v_lshl_add_u64 v[152:153], s[36:37], 0, v[154:155]
	v_pk_mul_f32 v[84:85], v[84:85], v[168:169]
	v_pk_mul_f32 v[86:87], v[86:87], v[166:167]
	v_pk_mul_f32 v[80:81], v[80:81], v[162:163]
	s_and_b64 vcc, exec, s[44:45]
	v_lshl_add_u64 v[152:153], v[140:141], 1, v[152:153]
	s_cbranch_vccz .Ltz3_13

.LBB0_930:
	v_pk_mul_f32 v[52:53], v[52:53], v[168:169]
	v_pk_mul_f32 v[54:55], v[54:55], v[166:167]
	v_pk_mul_f32 v[48:49], v[48:49], v[164:165]
	s_and_b64 vcc, exec, s[44:45]
	v_pk_mul_f32 v[50:51], v[50:51], v[150:151]
	s_cbranch_vccz .Ltz3_15

.LBB0_940:
	s_waitcnt vmcnt(0)
	v_cvt_f32_ubyte1_e32 v157, v158
	v_cvt_f32_ubyte0_e32 v156, v158
	v_cvt_f32_ubyte3_e32 v163, v158
	v_cvt_f32_ubyte2_e32 v162, v158
	v_cvt_f32_ubyte1_e32 v165, v159
	v_cvt_f32_ubyte0_e32 v164, v159
	v_cvt_f32_ubyte3_e32 v167, v159
	v_cvt_f32_ubyte2_e32 v166, v159
	s_and_b64 vcc, exec, s[42:43]
	s_mov_b64 s[2:3], -1
	s_cbranch_vccz .Ltz3_16

.LBB0_944:
	v_lshlrev_b64 v[156:157], 11, v[142:143]
	v_lshl_add_u64 v[156:157], v[156:157], 0, s[60:61]
	v_lshl_add_u64 v[156:157], s[36:37], 0, v[156:157]
	v_pk_mul_f32 v[44:45], v[44:45], v[172:173]
	v_pk_mul_f32 v[46:47], v[46:47], v[170:171]
	v_pk_mul_f32 v[40:41], v[40:41], v[168:169]
	v_pk_mul_f32 v[42:43], v[42:43], v[158:159]
	s_and_b64 vcc, exec, s[44:45]
	v_lshl_add_u64 v[156:157], v[140:141], 1, v[156:157]
	s_cbranch_vccz .Ltz3_17

.LBB0_950:
	v_pk_mul_f32 v[12:13], v[12:13], v[172:173]
	v_pk_mul_f32 v[14:15], v[14:15], v[170:171]
	v_pk_mul_f32 v[8:9], v[8:9], v[168:169]
	s_and_b64 vcc, exec, s[44:45]
	v_pk_mul_f32 v[10:11], v[10:11], v[154:155]
	s_cbranch_vccz .Ltz3_19

.LBB0_956:
	v_lshlrev_b64 v[154:155], 11, v[142:143]
	s_mov_b64 s[2:3], 0x48000
	v_lshl_add_u64 v[154:155], v[154:155], 0, s[2:3]
	v_pk_mul_f32 v[34:35], v[34:35], v[152:153]
	v_lshl_add_u64 v[152:153], s[36:37], 0, v[154:155]
	v_pk_mul_f32 v[36:37], v[36:37], v[168:169]
	v_pk_mul_f32 v[38:39], v[38:39], v[166:167]
	v_pk_mul_f32 v[32:33], v[32:33], v[162:163]
	s_and_b64 vcc, exec, s[44:45]
	v_lshl_add_u64 v[152:153], v[140:141], 1, v[152:153]
	s_cbranch_vccz .Ltz3_21

.LBB0_962:
	v_pk_mul_f32 v[4:5], v[4:5], v[168:169]
	v_pk_mul_f32 v[6:7], v[6:7], v[166:167]
	v_pk_mul_f32 v[0:1], v[0:1], v[164:165]
	s_and_b64 vcc, exec, s[44:45]
	v_pk_mul_f32 v[2:3], v[2:3], v[150:151]
	s_cbranch_vccz .Ltz3_23

.LBB0_972:
	s_waitcnt vmcnt(0)
	v_cvt_f32_ubyte1_e32 v155, v156
	v_cvt_f32_ubyte0_e32 v154, v156
	v_cvt_f32_ubyte3_e32 v159, v156
	v_cvt_f32_ubyte2_e32 v158, v156
	v_cvt_f32_ubyte1_e32 v163, v157
	v_cvt_f32_ubyte0_e32 v162, v157
	v_cvt_f32_ubyte3_e32 v167, v157
	v_cvt_f32_ubyte2_e32 v166, v157
	s_and_b64 vcc, exec, s[42:43]
	s_mov_b64 s[2:3], -1
	s_cbranch_vccz .Ltz3_24

.LBB0_976:
	v_lshlrev_b64 v[146:147], 11, v[142:143]
	s_mov_b64 s[2:3], 0x50000
	v_lshl_add_u64 v[146:147], v[146:147], 0, s[2:3]
	v_lshl_add_u64 v[146:147], s[36:37], 0, v[146:147]
	v_pk_mul_f32 v[28:29], v[28:29], v[170:171]
	v_pk_mul_f32 v[30:31], v[30:31], v[168:169]
	v_pk_mul_f32 v[24:25], v[24:25], v[164:165]
	v_pk_mul_f32 v[26:27], v[26:27], v[156:157]
	s_and_b64 vcc, exec, s[44:45]
	v_lshl_add_u64 v[146:147], v[140:141], 1, v[146:147]
	s_cbranch_vccz .Ltz3_25
.LBB0_978:
	s_nop 1
	v_cvt_f32_ubyte1_e32 v155, v152
	v_cvt_f32_ubyte0_e32 v154, v152
	v_cvt_f32_ubyte3_e32 v157, v152
	v_cvt_f32_ubyte2_e32 v156, v152
	v_cvt_f32_ubyte1_e32 v159, v153
	v_cvt_f32_ubyte0_e32 v158, v153
	v_cvt_f32_ubyte3_e32 v163, v153
	v_cvt_f32_ubyte2_e32 v162, v153
	s_and_b64 vcc, exec, s[42:43]
	s_mov_b64 s[2:3], -1
	s_cbranch_vccz .Ltz3_26

.LBB0_982:
	v_pk_mul_f32 v[112:113], v[112:113], v[168:169]
	v_pk_mul_f32 v[114:115], v[114:115], v[166:167]
	v_pk_mul_f32 v[116:117], v[116:117], v[164:165]
	s_and_b64 vcc, exec, s[44:45]
	v_pk_mul_f32 v[118:119], v[118:119], v[152:153]
	s_cbranch_vccz .Ltz3_27
.LBB0_984:
	v_cvt_f32_ubyte1_e32 v145, v150
	v_cvt_f32_ubyte0_e32 v144, v150
	v_cvt_f32_ubyte3_e32 v153, v150
	v_cvt_f32_ubyte2_e32 v152, v150
	v_cvt_f32_ubyte1_e32 v155, v151
	v_cvt_f32_ubyte0_e32 v154, v151
	v_cvt_f32_ubyte3_e32 v157, v151
	v_cvt_f32_ubyte2_e32 v156, v151
	s_and_b64 vcc, exec, s[42:43]
	s_mov_b64 s[2:3], -1
	s_cbranch_vccz .Ltz3_28

.LBB0_988:
	v_lshlrev_b64 v[138:139], 11, v[142:143]
	s_mov_b64 s[2:3], 0x58000
	v_lshl_add_u64 v[138:139], v[138:139], 0, s[2:3]
	v_lshl_add_u64 v[138:139], s[36:37], 0, v[138:139]
	v_pk_mul_f32 v[20:21], v[20:21], v[162:163]
	v_pk_mul_f32 v[22:23], v[22:23], v[158:159]
	v_pk_mul_f32 v[16:17], v[16:17], v[150:151]
	v_pk_mul_f32 v[18:19], v[18:19], v[146:147]
	s_and_b64 vcc, exec, s[44:45]
	v_lshl_add_u64 v[138:139], v[140:141], 1, v[138:139]
	s_cbranch_vccz .Ltz3_29
.LBB0_990:
	s_nop 1
	v_cvt_f32_ubyte1_e32 v141, v148
	v_cvt_f32_ubyte0_e32 v140, v148
	v_cvt_f32_ubyte3_e32 v143, v148
	v_cvt_f32_ubyte2_e32 v142, v148
	v_cvt_f32_ubyte1_e32 v147, v149
	v_cvt_f32_ubyte0_e32 v146, v149
	v_cvt_f32_ubyte3_e32 v151, v149
	v_cvt_f32_ubyte2_e32 v150, v149
	s_and_b64 vcc, exec, s[42:43]
	s_mov_b64 s[2:3], -1
	s_cbranch_vccz .Ltz3_30

.LBB0_994:
	v_pk_mul_f32 v[120:121], v[120:121], v[154:155]
	v_pk_mul_f32 v[122:123], v[122:123], v[152:153]
	v_pk_mul_f32 v[124:125], v[124:125], v[148:149]
	s_and_b64 vcc, exec, s[44:45]
	v_pk_mul_f32 v[126:127], v[126:127], v[144:145]
	s_cbranch_vccz .Ltz3_31

.Ltz3_0:
	v_pk_mul_f32 v[156:157], v[166:167], s[82:83] op_sel_hi:[1,0]
	v_pk_mul_f32 v[158:159], v[162:163], s[82:83] op_sel_hi:[1,0]
	v_pk_mul_f32 v[164:165], v[142:143], s[82:83] op_sel_hi:[1,0]
	v_pk_mul_f32 v[168:169], v[140:141], s[82:83] op_sel_hi:[1,0]
	s_mov_b64 s[2:3], 0
	s_branch .LBB0_876
.Ltz3_1:
	v_cvt_pk_bf16_f32 v162, v108, v109
	v_cvt_pk_bf16_f32 v163, v110, v111
	v_cvt_pk_bf16_f32 v164, v104, v105
	v_cvt_pk_bf16_f32 v165, v106, v107
	global_store_dwordx4 v[156:157], v[162:165], off
	s_branch .LBB0_880
.Ltz3_2:
	v_pk_mul_f32 v[154:155], v[166:167], s[82:83] op_sel_hi:[1,0]
	v_pk_mul_f32 v[168:169], v[164:165], s[82:83] op_sel_hi:[1,0]
	v_pk_mul_f32 v[170:171], v[162:163], s[82:83] op_sel_hi:[1,0]
	v_pk_mul_f32 v[172:173], v[158:159], s[82:83] op_sel_hi:[1,0]
	s_mov_b64 s[22:23], 0
	s_branch .LBB0_882
.Ltz3_3:
	v_cvt_pk_bf16_f32 v162, v76, v77
	v_cvt_pk_bf16_f32 v163, v78, v79
	v_cvt_pk_bf16_f32 v164, v72, v73
	v_cvt_pk_bf16_f32 v165, v74, v75
	global_store_dwordx4 v[156:157], v[162:165], off offset:256
	s_branch .LBB0_886
.Ltz3_4:
	v_pk_mul_f32 v[152:153], v[164:165], s[82:83] op_sel_hi:[1,0]
	v_pk_mul_f32 v[162:163], v[158:159], s[82:83] op_sel_hi:[1,0]
	v_pk_mul_f32 v[166:167], v[156:157], s[82:83] op_sel_hi:[1,0]
	v_pk_mul_f32 v[168:169], v[154:155], s[82:83] op_sel_hi:[1,0]
	s_mov_b64 s[2:3], 0
	s_branch .LBB0_888
.Ltz3_5:
	v_cvt_pk_bf16_f32 v154, v100, v101
	v_cvt_pk_bf16_f32 v155, v102, v103
	v_cvt_pk_bf16_f32 v156, v96, v97
	v_cvt_pk_bf16_f32 v157, v98, v99
	global_store_dwordx4 v[152:153], v[154:157], off
	s_branch .LBB0_892
.Ltz3_6:
	v_pk_mul_f32 v[150:151], v[162:163], s[82:83] op_sel_hi:[1,0]
	v_pk_mul_f32 v[164:165], v[158:159], s[82:83] op_sel_hi:[1,0]
	v_pk_mul_f32 v[166:167], v[156:157], s[82:83] op_sel_hi:[1,0]
	v_pk_mul_f32 v[168:169], v[154:155], s[82:83] op_sel_hi:[1,0]
	s_mov_b64 s[2:3], 0
	s_branch .LBB0_894
.Ltz3_7:
	v_cvt_pk_bf16_f32 v154, v68, v69
	v_cvt_pk_bf16_f32 v155, v70, v71
	v_cvt_pk_bf16_f32 v156, v64, v65
	v_cvt_pk_bf16_f32 v157, v66, v67
	global_store_dwordx4 v[152:153], v[154:157], off offset:256
	s_branch .LBB0_898
.Ltz3_8:
	v_pk_mul_f32 v[158:159], v[168:169], s[82:83] op_sel_hi:[1,0]
	v_pk_mul_f32 v[166:167], v[164:165], s[82:83] op_sel_hi:[1,0]
	v_pk_mul_f32 v[170:171], v[162:163], s[82:83] op_sel_hi:[1,0]
	v_pk_mul_f32 v[172:173], v[156:157], s[82:83] op_sel_hi:[1,0]
	s_mov_b64 s[2:3], 0
	s_branch .LBB0_910
.Ltz3_9:
	v_cvt_pk_bf16_f32 v162, v92, v93
	v_cvt_pk_bf16_f32 v163, v94, v95
	v_cvt_pk_bf16_f32 v164, v88, v89
	v_cvt_pk_bf16_f32 v165, v90, v91
	global_store_dwordx4 v[156:157], v[162:165], off
	s_branch .LBB0_914
.Ltz3_10:
	v_pk_mul_f32 v[154:155], v[166:167], s[82:83] op_sel_hi:[1,0]
	v_pk_mul_f32 v[168:169], v[164:165], s[82:83] op_sel_hi:[1,0]
	v_pk_mul_f32 v[170:171], v[162:163], s[82:83] op_sel_hi:[1,0]
	v_pk_mul_f32 v[172:173], v[158:159], s[82:83] op_sel_hi:[1,0]
	s_mov_b64 s[2:3], 0
	s_branch .LBB0_916
.Ltz3_11:
	v_cvt_pk_bf16_f32 v162, v60, v61
	v_cvt_pk_bf16_f32 v163, v62, v63
	v_cvt_pk_bf16_f32 v164, v56, v57
	v_cvt_pk_bf16_f32 v165, v58, v59
	global_store_dwordx4 v[156:157], v[162:165], off offset:256
	s_branch .LBB0_920

.Ltz3_13:
	v_cvt_pk_bf16_f32 v154, v84, v85
	v_cvt_pk_bf16_f32 v155, v86, v87
	v_cvt_pk_bf16_f32 v156, v80, v81
	v_cvt_pk_bf16_f32 v157, v82, v83
	global_store_dwordx4 v[152:153], v[154:157], off
	s_branch .LBB0_926

.Ltz3_15:
	v_cvt_pk_bf16_f32 v154, v52, v53
	v_cvt_pk_bf16_f32 v155, v54, v55
	v_cvt_pk_bf16_f32 v156, v48, v49
	v_cvt_pk_bf16_f32 v157, v50, v51
	global_store_dwordx4 v[152:153], v[154:157], off offset:256
	s_branch .LBB0_932
.Ltz3_16:
	v_pk_mul_f32 v[158:159], v[166:167], s[82:83] op_sel_hi:[1,0]
	v_pk_mul_f32 v[168:169], v[164:165], s[82:83] op_sel_hi:[1,0]
	v_pk_mul_f32 v[170:171], v[162:163], s[82:83] op_sel_hi:[1,0]
	v_pk_mul_f32 v[172:173], v[156:157], s[82:83] op_sel_hi:[1,0]
	s_mov_b64 s[2:3], 0
	s_branch .LBB0_942
.Ltz3_17:
	v_cvt_pk_bf16_f32 v162, v44, v45
	v_cvt_pk_bf16_f32 v163, v46, v47
	v_cvt_pk_bf16_f32 v164, v40, v41
	v_cvt_pk_bf16_f32 v165, v42, v43
	global_store_dwordx4 v[156:157], v[162:165], off
	s_branch .LBB0_946

.Ltz3_19:
	v_cvt_pk_bf16_f32 v162, v12, v13
	v_cvt_pk_bf16_f32 v163, v14, v15
	v_cvt_pk_bf16_f32 v164, v8, v9
	v_cvt_pk_bf16_f32 v165, v10, v11
	global_store_dwordx4 v[156:157], v[162:165], off offset:256
	s_branch .LBB0_952

.Ltz3_21:
	v_cvt_pk_bf16_f32 v154, v36, v37
	v_cvt_pk_bf16_f32 v155, v38, v39
	v_cvt_pk_bf16_f32 v156, v32, v33
	v_cvt_pk_bf16_f32 v157, v34, v35
	global_store_dwordx4 v[152:153], v[154:157], off
	s_branch .LBB0_958

.Ltz3_23:
	v_cvt_pk_bf16_f32 v154, v4, v5
	v_cvt_pk_bf16_f32 v155, v6, v7
	v_cvt_pk_bf16_f32 v156, v0, v1
	v_cvt_pk_bf16_f32 v157, v2, v3
	global_store_dwordx4 v[152:153], v[154:157], off offset:256
	s_branch .LBB0_964
.Ltz3_24:
	v_pk_mul_f32 v[156:157], v[166:167], s[82:83] op_sel_hi:[1,0]
	v_pk_mul_f32 v[164:165], v[162:163], s[82:83] op_sel_hi:[1,0]
	v_pk_mul_f32 v[168:169], v[158:159], s[82:83] op_sel_hi:[1,0]
	v_pk_mul_f32 v[170:171], v[154:155], s[82:83] op_sel_hi:[1,0]
	s_mov_b64 s[2:3], 0
	s_branch .LBB0_974
.Ltz3_25:
	v_cvt_pk_bf16_f32 v154, v28, v29
	v_cvt_pk_bf16_f32 v155, v30, v31
	v_cvt_pk_bf16_f32 v156, v24, v25
	v_cvt_pk_bf16_f32 v157, v26, v27
	global_store_dwordx4 v[146:147], v[154:157], off
	s_branch .LBB0_978
.Ltz3_26:
	v_pk_mul_f32 v[152:153], v[162:163], s[82:83] op_sel_hi:[1,0]
	v_pk_mul_f32 v[164:165], v[158:159], s[82:83] op_sel_hi:[1,0]
	v_pk_mul_f32 v[166:167], v[156:157], s[82:83] op_sel_hi:[1,0]
	v_pk_mul_f32 v[168:169], v[154:155], s[82:83] op_sel_hi:[1,0]
	s_mov_b64 s[2:3], 0
	s_branch .LBB0_980
.Ltz3_27:
	v_cvt_pk_bf16_f32 v152, v112, v113
	v_cvt_pk_bf16_f32 v153, v114, v115
	v_cvt_pk_bf16_f32 v154, v116, v117
	v_cvt_pk_bf16_f32 v155, v118, v119
	global_store_dwordx4 v[146:147], v[152:155], off offset:256
	s_branch .LBB0_984
.Ltz3_28:
	v_pk_mul_f32 v[146:147], v[156:157], s[82:83] op_sel_hi:[1,0]
	v_pk_mul_f32 v[150:151], v[154:155], s[82:83] op_sel_hi:[1,0]
	v_pk_mul_f32 v[158:159], v[152:153], s[82:83] op_sel_hi:[1,0]
	v_pk_mul_f32 v[162:163], v[144:145], s[82:83] op_sel_hi:[1,0]
	s_mov_b64 s[2:3], 0
	s_branch .LBB0_986
.Ltz3_29:
	v_cvt_pk_bf16_f32 v140, v20, v21
	v_cvt_pk_bf16_f32 v141, v22, v23
	v_cvt_pk_bf16_f32 v142, v16, v17
	v_cvt_pk_bf16_f32 v143, v18, v19
	global_store_dwordx4 v[138:139], v[140:143], off
	s_branch .LBB0_990
.Ltz3_30:
	v_pk_mul_f32 v[144:145], v[150:151], s[82:83] op_sel_hi:[1,0]
	v_pk_mul_f32 v[148:149], v[146:147], s[82:83] op_sel_hi:[1,0]
	v_pk_mul_f32 v[152:153], v[142:143], s[82:83] op_sel_hi:[1,0]
	v_pk_mul_f32 v[154:155], v[140:141], s[82:83] op_sel_hi:[1,0]
	s_mov_b64 s[2:3], 0
	s_branch .LBB0_992
.Ltz3_31:
	v_cvt_pk_bf16_f32 v140, v120, v121
	v_cvt_pk_bf16_f32 v141, v122, v123
	v_cvt_pk_bf16_f32 v142, v124, v125
	v_cvt_pk_bf16_f32 v143, v126, v127
	global_store_dwordx4 v[138:139], v[140:143], off offset:256
	s_branch .LBB0_996
